# far selected blocks: software-pipelined block-major items (8+4 fragment slots, in-place P packing), O/l parked in LDS rows, Q prefetch kept in flight across the step barrier
# speedup vs baseline: 1.0049x; 1.0049x over previous
; #define LAS __attribute__((address_space(3)))
; __device__ __forceinline__ unsigned or_x16(unsigned u) { return u | __shfl_xor(u, 16); }
; __device__ __forceinline__ unsigned or_x32(unsigned u) { return u | __shfl_xor(u, 32); }
; __device__ __forceinline__ void select_blocks8(const LAS float* impw, LAS unsigned* mk, int lane, int cur, unsigned (&u)[2][4]) {
;     ...
; #pragma unroll
;     for (int c = 0; c < 2; ++c) {
;         if (i == 0) *(LAS u32x4*)(mk + (4 * c + k) * 4) = (u32x4){m4[c][0], m4[c][1], m4[c][2], m4[c][3]};
; #pragma unroll
;         for (int x = 0; x < 4; ++x) { unsigned v = m4[c][x]; v = or_x16(v); v = or_x32(v); u[c][x] = __builtin_amdgcn_readfirstlane(v); }
;     }
; __device__ __forceinline__ void nsa_unit(unsigned char* ws, LAS unsigned char* lds, const LAS float* lut, int b, int g, int tau, int tid_in) {
;     ...
; #pragma unroll
;     for (int c = 0; c < 2; ++c) { const float gc = NSA_GATE(c, 0);
; #pragma unroll
;         for (int dt = 0; dt < 4; ++dt) resw[(c * 4 + dt) * 64] = Oc[c][dt] * gc; }
.LBB0_1173:
	s_lshl_b32 s1, s91, 7
	s_add_i32 s24, s1, 0
	s_add_i32 s24, s24, 0x22d00
	v_cmp_eq_u32_e32 vcc, 0, v187
	v_add_u32_e32 v4, s24, v1
	s_and_saveexec_b64 s[6:7], vcc
	ds_write_b128 v4, v[74:77]
	s_or_b64 exec, exec, s[6:7]
	v_and_b32_e32 v5, 64, v176
	v_xor_b32_e32 v3, 16, v176
	v_add_u32_e32 v5, 64, v5
	v_cmp_lt_i32_e64 s[6:7], v3, v5
	v_xor_b32_e32 v78, 32, v176
	s_nop 0
	v_cndmask_b32_e64 v3, v176, v3, s[6:7]
	v_cmp_lt_i32_e64 s[6:7], v78, v5
	v_lshlrev_b32_e32 v3, 2, v3
	s_nop 0
	v_cndmask_b32_e64 v5, v176, v78, s[6:7]
	v_lshlrev_b32_e32 v155, 2, v5
	ds_bpermute_b32 v5, v3, v74
	s_waitcnt lgkmcnt(0)
	v_or_b32_e32 v5, v5, v74
	ds_bpermute_b32 v74, v155, v5
	s_waitcnt lgkmcnt(0)
	v_or_b32_e32 v5, v74, v5
	s_nop 0
	v_readfirstlane_b32 s17, v5
	ds_bpermute_b32 v5, v3, v75
	s_waitcnt lgkmcnt(0)
	v_or_b32_e32 v5, v5, v75
	ds_bpermute_b32 v74, v155, v5
	s_waitcnt lgkmcnt(0)
	v_or_b32_e32 v5, v74, v5
	s_nop 0
	v_readfirstlane_b32 s38, v5
	ds_bpermute_b32 v5, v3, v76
	s_waitcnt lgkmcnt(0)
	v_or_b32_e32 v5, v5, v76
	ds_bpermute_b32 v74, v155, v5
	s_waitcnt lgkmcnt(0)
	v_or_b32_e32 v5, v74, v5
	s_nop 0
	v_readfirstlane_b32 s39, v5
	ds_bpermute_b32 v5, v3, v77
	s_waitcnt lgkmcnt(0)
	v_or_b32_e32 v5, v5, v77
	ds_bpermute_b32 v74, v155, v5
	s_waitcnt lgkmcnt(0)
	v_or_b32_e32 v5, v74, v5
	s_nop 0
	v_readfirstlane_b32 s5, v5
	s_and_saveexec_b64 s[6:7], vcc
	ds_write_b128 v4, v[70:73] offset:64
	s_or_b64 exec, exec, s[6:7]
	ds_bpermute_b32 v4, v3, v70
	s_lshl_b32 s6, s2, 13
	s_mov_b32 s7, s27
	v_lshl_add_u64 v[158:159], s[6:7], 0, v[164:165]
	s_waitcnt lgkmcnt(0)
	v_or_b32_e32 v4, v4, v70
	ds_bpermute_b32 v5, v155, v4
	s_barrier
	s_waitcnt lgkmcnt(0)
	s_lshl_b32 s1, s91, 13
	s_add_i32 s1, s1, 0
	v_or_b32_e32 v74, v5, v4
	ds_bpermute_b32 v4, v3, v71
	v_lshl_add_u32 v1, v1, 4, s1
	v_add_u32_e32 v1, 0x10000, v1
	s_movk_i32 s1, 0x70
	s_andn2_b64 vcc, exec, s[50:51]
	s_waitcnt lgkmcnt(0)
	v_or_b32_e32 v4, v4, v71
	ds_bpermute_b32 v5, v155, v4
	s_waitcnt lgkmcnt(0)
	v_or_b32_e32 v75, v5, v4
	ds_bpermute_b32 v4, v3, v72
	v_readfirstlane_b32 s73, v75
	s_waitcnt lgkmcnt(0)
	v_or_b32_e32 v4, v4, v72
	ds_bpermute_b32 v5, v155, v4
	s_waitcnt lgkmcnt(0)
	v_or_b32_e32 v72, v5, v4
	ds_bpermute_b32 v4, v3, v73
	s_waitcnt lgkmcnt(0)
	v_or_b32_e32 v4, v4, v73
	ds_bpermute_b32 v5, v155, v4
	s_waitcnt lgkmcnt(0)
	v_or_b32_e32 v73, v5, v4
	v_mul_u32_u24_e32 v4, 3, v191
	v_lshlrev_b32_e32 v152, 2, v4
	v_lshl_add_u64 v[70:71], s[28:29], 0, v[152:153]
	v_mad_u64_u32 v[4:5], s[2:3], v158, s0, v[70:71]
	v_mad_i32_i24 v5, v159, s0, v5
	global_load_dword v4, v[4:5], off
	v_readfirstlane_b32 s72, v73
	s_waitcnt vmcnt(0)
	v_pk_mul_f32 v[212:213], v[56:57], v[4:5] op_sel_hi:[1,0]
	v_pk_mul_f32 v[210:211], v[54:55], v[4:5] op_sel_hi:[1,0]
	v_pk_mul_f32 v[216:217], v[60:61], v[4:5] op_sel_hi:[1,0]
	v_pk_mul_f32 v[214:215], v[58:59], v[4:5] op_sel_hi:[1,0]
	v_pk_mul_f32 v[220:221], v[64:65], v[4:5] op_sel_hi:[1,0]
	v_pk_mul_f32 v[218:219], v[62:63], v[4:5] op_sel_hi:[1,0]
	v_pk_mul_f32 v[224:225], v[68:69], v[4:5] op_sel_hi:[1,0]
	v_pk_mul_f32 v[222:223], v[66:67], v[4:5] op_sel_hi:[1,0]
	v_lshl_add_u64 v[4:5], s[6:7], 0, v[108:109]
	v_mad_u64_u32 v[54:55], s[2:3], v4, s0, v[70:71]
	v_mad_i32_i24 v55, v5, s0, v55
	global_load_dword v54, v[54:55], off
	v_readfirstlane_b32 s2, v74
	v_readfirstlane_b32 s3, v72
	s_waitcnt vmcnt(0)
	v_pk_mul_f32 v[228:229], v[40:41], v[54:55] op_sel_hi:[1,0]
	v_pk_mul_f32 v[226:227], v[38:39], v[54:55] op_sel_hi:[1,0]
	v_pk_mul_f32 v[232:233], v[44:45], v[54:55] op_sel_hi:[1,0]
	v_pk_mul_f32 v[230:231], v[42:43], v[54:55] op_sel_hi:[1,0]
	v_pk_mul_f32 v[236:237], v[48:49], v[54:55] op_sel_hi:[1,0]
	v_pk_mul_f32 v[234:235], v[46:47], v[54:55] op_sel_hi:[1,0]
	v_pk_mul_f32 v[240:241], v[52:53], v[54:55] op_sel_hi:[1,0]
	v_pk_mul_f32 v[238:239], v[50:51], v[54:55] op_sel_hi:[1,0]
	s_mov_b32 s98, 0
	s_mov_b32 s100, -1
	v_and_b32_e32 v248, 3, v185
	v_lshlrev_b32_e32 v249, 2, v248
	v_lshl_add_u32 v248, v186, 6, v249
	v_add_u32_e32 v248, 0x10000, v248
	v_add_u32_e32 v249, 0x20400, v249
	v_lshlrev_b32_e32 v250, 2, v184
	v_and_b32_e32 v251, 63, v185
	v_lshlrev_b32_e32 v251, 4, v251
	v_add_u32_e32 v251, 0x22d00, v251
	ds_read_b128 v[242:245], v251
	s_waitcnt lgkmcnt(0)
	v_xor_b32_e32 v39, v110, v185
	v_lshlrev_b32_e32 v38, 7, v110
	v_lshlrev_b32_e32 v39, 4, v39
	v_and_or_b32 v38, v39, s1, v38
	v_add_u32_e32 v188, 0, v38
	v_cndmask_b32_e64 v38, 0, 1, s[50:51]
	v_cmp_ne_u32_e64 s[6:7], 1, v38
	ds_write_b128 v188, v[26:29]
	ds_write_b128 v188, v[22:25] offset:32768
	s_cbranch_vccnz .LBB0_1179
	ds_write_b128 v188, v[30:33] offset:8192
	ds_write_b128 v188, v[34:37] offset:40960

.LBB0_1182:
	s_lshr_b32 s11, s75, 3
	s_waitcnt vmcnt(3)
	v_add_u32_e32 v22, s11, v165
	ds_read2_b32 v[174:175], v22 offset1:16
.LBB0_1183:
	s_add_i32 s76, s75, 2
	s_cmp_gt_i32 s76, s37
	s_cselect_b64 s[66:67], -1, 0
	s_cmp_le_i32 s76, s37
	s_cselect_b64 s[68:69], -1, 0
	s_and_b64 s[12:13], s[66:67], exec
	s_cselect_b32 s13, s79, s65
	s_cselect_b32 s12, s54, s64
	s_cselect_b32 s15, s36, s63
	s_cselect_b32 s14, s51, s62
	s_waitcnt vmcnt(3)
	v_lshl_add_u64 v[22:23], s[14:15], 0, v[162:163]
	s_waitcnt vmcnt(2)
	v_lshl_add_u64 v[26:27], s[12:13], 0, v[156:157]
	v_lshl_add_u64 v[22:23], v[22:23], 0, v[160:161]
	v_lshl_add_u64 v[26:27], v[26:27], 0, v[160:161]
	global_load_dwordx4 v[22:25], v[22:23], off
	s_add_i32 s11, s75, 3
	global_load_dwordx4 v[26:29], v[26:27], off
	s_cmp_le_i32 s11, s37
	s_cselect_b64 s[70:71], -1, 0
	s_cmp_gt_i32 s11, s37
	s_cbranch_scc1 .LBB0_1185
	v_lshl_add_u64 v[30:31], s[64:65], 0, v[166:167]
	v_add_co_u32_e32 v30, vcc, 0x8000, v30
	v_lshl_add_u64 v[34:35], s[62:63], 0, v[168:169]
	s_nop 0
	v_addc_co_u32_e32 v31, vcc, 0, v31, vcc
	global_load_dwordx4 v[30:33], v[30:31], off
	s_nop 0
	global_load_dwordx4 v[34:37], v[34:35], off offset:128
.LBB0_1185:
	s_cmp_lt_u32 s75, 2
	s_cbranch_scc1 .Lbm_old
	s_cmp_gt_i32 s75, s26
	s_cbranch_scc0 .Lbm_step
	s_cmp_eq_u32 s98, 0
	s_cbranch_scc1 .Lbm_old
	s_mul_i32 s11, s91, 8320
	v_mul_u32_u24_e32 v79, 260, v250
	v_add3_u32 v79, v79, s11, v248
	v_lshlrev_b32_e32 v80, 6, v186
	v_sub_u32_e32 v80, v79, v80
	ds_read_b32 v70, v79 offset:0
	ds_read_b32 v71, v79 offset:16
	ds_read_b32 v72, v79 offset:32
	ds_read_b32 v73, v79 offset:48
	ds_read_b32 v66, v79 offset:256
	ds_read_b32 v67, v79 offset:272
	ds_read_b32 v68, v79 offset:288
	ds_read_b32 v69, v79 offset:304
	ds_read_b32 v62, v79 offset:512
	ds_read_b32 v63, v79 offset:528
	ds_read_b32 v64, v79 offset:544
	ds_read_b32 v65, v79 offset:560
	s_waitcnt lgkmcnt(0)
	ds_read_b32 v54, v79 offset:768
	ds_read_b32 v55, v79 offset:784
	ds_read_b32 v56, v79 offset:800
	ds_read_b32 v57, v79 offset:816
	ds_read_b32 v50, v79 offset:4160
	ds_read_b32 v51, v79 offset:4176
	ds_read_b32 v52, v79 offset:4192
	ds_read_b32 v53, v79 offset:4208
	ds_read_b32 v46, v79 offset:4416
	ds_read_b32 v47, v79 offset:4432
	ds_read_b32 v48, v79 offset:4448
	ds_read_b32 v49, v79 offset:4464
	s_waitcnt lgkmcnt(0)
	ds_read_b32 v42, v79 offset:4672
	ds_read_b32 v43, v79 offset:4688
	ds_read_b32 v44, v79 offset:4704
	ds_read_b32 v45, v79 offset:4720
	ds_read_b32 v38, v79 offset:4928
	ds_read_b32 v39, v79 offset:4944
	ds_read_b32 v40, v79 offset:4960
	ds_read_b32 v41, v79 offset:4976
	ds_read_b32 v74, v80 offset:1024
	ds_read_b32 v58, v80 offset:5184
	s_waitcnt lgkmcnt(0)
	v_mov_b32_e32 v75, v74
	v_mov_b32_e32 v76, v74
	v_mov_b32_e32 v77, v74
	v_mov_b32_e32 v59, v58
	v_mov_b32_e32 v60, v58
	v_mov_b32_e32 v61, v58
	s_mov_b32 s98, 0

.LBB0_1224:
	s_cmp_lg_u32 s75, 0
	s_cbranch_scc1 .Lbm_nopub
	v_lshl_add_u32 v79, v250, 2, v249
	s_lshl_b32 s11, s91, 7
	v_add_u32_e32 v79, s11, v79
	ds_write_b32 v79, v198
	ds_write_b32 v79, v197 offset:64
	s_cmp_lt_i32 s26, 2
	s_cbranch_scc1 .Lbm_nopub
	s_mul_i32 s11, s91, 8320
	v_mul_u32_u24_e32 v79, 260, v250
	v_add3_u32 v79, v79, s11, v248
	v_lshlrev_b32_e32 v80, 6, v186
	v_sub_u32_e32 v80, v79, v80
	ds_write_b32 v79, v70 offset:0
	ds_write_b32 v79, v71 offset:16
	ds_write_b32 v79, v72 offset:32
	ds_write_b32 v79, v73 offset:48
	ds_write_b32 v79, v66 offset:256
	ds_write_b32 v79, v67 offset:272
	ds_write_b32 v79, v68 offset:288
	ds_write_b32 v79, v69 offset:304
	ds_write_b32 v79, v62 offset:512
	ds_write_b32 v79, v63 offset:528
	ds_write_b32 v79, v64 offset:544
	ds_write_b32 v79, v65 offset:560
	s_waitcnt lgkmcnt(0)
	ds_write_b32 v79, v54 offset:768
	ds_write_b32 v79, v55 offset:784
	ds_write_b32 v79, v56 offset:800
	ds_write_b32 v79, v57 offset:816
	ds_write_b32 v79, v50 offset:4160
	ds_write_b32 v79, v51 offset:4176
	ds_write_b32 v79, v52 offset:4192
	ds_write_b32 v79, v53 offset:4208
	ds_write_b32 v79, v46 offset:4416
	ds_write_b32 v79, v47 offset:4432
	ds_write_b32 v79, v48 offset:4448
	ds_write_b32 v79, v49 offset:4464
	s_waitcnt lgkmcnt(0)
	ds_write_b32 v79, v42 offset:4672
	ds_write_b32 v79, v43 offset:4688
	ds_write_b32 v79, v44 offset:4704
	ds_write_b32 v79, v45 offset:4720
	ds_write_b32 v79, v38 offset:4928
	ds_write_b32 v79, v39 offset:4944
	ds_write_b32 v79, v40 offset:4960
	ds_write_b32 v79, v41 offset:4976
	ds_write_b32 v80, v74 offset:1024
	ds_write_b32 v80, v58 offset:5184

; #define LAS __attribute__((address_space(3)))
; __device__ __forceinline__ float ex2(float x) { return __builtin_amdgcn_exp2f(x); }
; template <bool SELMASK>
; __device__ __forceinline__ void attn_far_fast(const LAS unsigned char* kb, const LAS unsigned char* vb, const bf16x8 (&qf)[2][2], int col, int q, float bias_far, bool sel0, bool sel1, Softmax (&st)[2], f32x4 (&O)[2][4]) {
;     const f32x4 z4 = (f32x4){0.f, 0.f, 0.f, 0.f};
;     const float NEG = -__builtin_inff();
;     f32x4 S[2][4];
; #pragma unroll
;     for (int kt = 0; kt < 4; ++kt) { const bf16x8 k0 = lds_frag(kb, 16 * kt + col, q), k1 = lds_frag(kb, 16 * kt + col, 4 + q);
; #pragma unroll
;         for (int c = 0; c < 2; ++c) { S[c][kt] = __builtin_amdgcn_mfma_f32_16x16x32_bf16(k0, qf[c][0], z4, 0, 0, 0); S[c][kt] = __builtin_amdgcn_mfma_f32_16x16x32_bf16(k1, qf[c][1], S[c][kt], 0, 0, 0); } }
;     bf16x8 pf[2][2];
; #pragma unroll
;     for (int c = 0; c < 2; ++c) {
;         const bool sel = c == 0 ? sel0 : sel1;
;         const float off = ((SELMASK && !sel) ? NEG : bias_far) - st[c].m;
; #pragma unroll
;         for (int kt = 0; kt < 4; ++kt) { f32x4 p = S[c][kt] + off;
; #pragma unroll
;             for (int e = 0; e < 4; ++e) p[e] = ex2(p[e]);
;             S[c][kt] = p; }
;         pf[c][0] = pack8(S[c][0], S[c][1]); pf[c][1] = pack8(S[c][2], S[c][3]);
;         st[c].l = __builtin_amdgcn_mfma_f32_16x16x32_bf16(ONES8, pf[c][0], st[c].l, 0, 0, 0); st[c].l = __builtin_amdgcn_mfma_f32_16x16x32_bf16(ONES8, pf[c][1], st[c].l, 0, 0, 0);
;     }
.Lbm_r1_go:
	s_cmp_eq_u32 s101, 1
	s_cbranch_scc1 .Lbm_r1_two
	v_add_u32_e32 v148, s83, v192
	v_add_u32_e32 v149, v148, v195
	v_add_u32_e32 v148, v148, v193
	v_add_u32_e32 v208, s99, v192
	v_add_u32_e32 v209, v208, v195
	v_add_u32_e32 v208, v208, v193
	ds_read_b128 v[116:119], v148
	ds_read_b128 v[120:123], v149
	ds_read_b128 v[124:127], v148 offset:2048
	ds_read_b128 v[128:131], v149 offset:2048
	ds_read_b128 v[132:135], v148 offset:4096
	ds_read_b128 v[136:139], v149 offset:4096
	ds_read_b128 v[140:143], v148 offset:6144
	ds_read_b128 v[144:147], v149 offset:6144
	v_mov_b32_e32 v70, v81
	v_mov_b32_e32 v71, v81
	v_mov_b32_e32 v72, v81
	v_mov_b32_e32 v73, v81
	v_mov_b32_e32 v74, v81
	v_mov_b32_e32 v75, v81
	v_mov_b32_e32 v76, v81
	v_mov_b32_e32 v77, v81
	v_mov_b32_e32 v200, v81
	v_mov_b32_e32 v201, v81
	v_mov_b32_e32 v202, v81
	v_mov_b32_e32 v203, v81
	v_mov_b32_e32 v204, v81
	v_mov_b32_e32 v205, v81
	v_mov_b32_e32 v206, v81
	v_mov_b32_e32 v207, v81
	ds_read_b128 v[38:41], v208
	ds_read_b128 v[42:45], v209
	ds_read_b128 v[46:49], v208 offset:2048
	ds_read_b128 v[50:53], v209 offset:2048
	v_mov_b32_e32 v54, v82
	v_mov_b32_e32 v55, v82
	v_mov_b32_e32 v56, v82
	v_mov_b32_e32 v57, v82
	v_mov_b32_e32 v58, v82
	v_mov_b32_e32 v59, v82
	v_mov_b32_e32 v60, v82
	v_mov_b32_e32 v61, v82
	v_mov_b32_e32 v62, v82
	v_mov_b32_e32 v63, v82
	v_mov_b32_e32 v64, v82
	v_mov_b32_e32 v65, v82
	v_mov_b32_e32 v66, v82
	v_mov_b32_e32 v67, v82
	v_mov_b32_e32 v68, v82
	v_mov_b32_e32 v69, v82
	s_mov_b32 s83, -1
	s_add_i32 s77, s75, 2
	s_cmp_gt_i32 s77, s26
	s_cbranch_scc1 .Lbm_g1_end_a
	s_lshr_b32 s21, s77, 5
	v_mov_b32_e32 v255, v242
	s_cmp_eq_u32 s21, 1
	s_cselect_b64 vcc, -1, 0
	v_cndmask_b32_e32 v255, v255, v243, vcc
	s_cmp_eq_u32 s21, 2
	s_cselect_b64 vcc, -1, 0
	v_cndmask_b32_e32 v255, v255, v244, vcc
	s_cmp_eq_u32 s21, 3
	s_cselect_b64 vcc, -1, 0
	v_cndmask_b32_e32 v255, v255, v245, vcc
	s_and_b32 s21, s77, 31
	s_lshl_b32 s21, 1, s21
	s_lshl_b32 s32, s21, 1
	v_and_b32_e32 v80, s21, v255
	v_cmp_ne_u32_e64 s[12:13], 0, v80
	v_and_b32_e32 v80, s32, v255
	v_cmp_ne_u32_e64 s[14:15], 0, v80
	s_nop 3
	s_or_b64 s[22:23], s[12:13], s[14:15]
	s_bcnt1_i32_b64 s11, s[22:23]
	s_add_i32 s11, s11, 3
	s_lshr_b32 s11, s11, 2
	s_cmp_ge_u32 s91, s11
	s_cbranch_scc1 .Lbm_g1_end_a
	s_add_i32 s83, s75, 2
.Lbm_g1_end_a:
	s_waitcnt lgkmcnt(10)
	v_mfma_f32_16x16x32_bf16 v[70:73], v[116:119], v[104:107], v[70:73]
	v_mfma_f32_16x16x32_bf16 v[70:73], v[120:123], v[108:111], v[70:73]
	s_waitcnt lgkmcnt(8)
	v_mfma_f32_16x16x32_bf16 v[74:77], v[124:127], v[104:107], v[74:77]
	v_mfma_f32_16x16x32_bf16 v[74:77], v[128:131], v[108:111], v[74:77]
	ds_read_b128 v[116:119], v148 offset:32768
	ds_read_b128 v[120:123], v149 offset:32768
	ds_read_b128 v[124:127], v148 offset:34816
	ds_read_b128 v[128:131], v149 offset:34816
	s_waitcnt lgkmcnt(10)
	v_mfma_f32_16x16x32_bf16 v[200:203], v[132:135], v[104:107], v[200:203]
	v_mfma_f32_16x16x32_bf16 v[200:203], v[136:139], v[108:111], v[200:203]
	s_waitcnt lgkmcnt(8)
	v_mfma_f32_16x16x32_bf16 v[204:207], v[140:143], v[104:107], v[204:207]
	v_mfma_f32_16x16x32_bf16 v[204:207], v[144:147], v[108:111], v[204:207]
	ds_read_b128 v[132:135], v148 offset:36864
	ds_read_b128 v[136:139], v149 offset:36864
	ds_read_b128 v[140:143], v148 offset:38912
	ds_read_b128 v[144:147], v149 offset:38912
	s_waitcnt lgkmcnt(10)
	v_mfma_f32_16x16x32_bf16 v[54:57], v[38:41], v[104:107], v[54:57]
	v_mfma_f32_16x16x32_bf16 v[54:57], v[42:45], v[108:111], v[54:57]
	s_waitcnt lgkmcnt(8)
	v_mfma_f32_16x16x32_bf16 v[58:61], v[46:49], v[104:107], v[58:61]
	v_mfma_f32_16x16x32_bf16 v[58:61], v[50:53], v[108:111], v[58:61]
	ds_read_b128 v[38:41], v208 offset:4096
	ds_read_b128 v[42:45], v209 offset:4096
	ds_read_b128 v[46:49], v208 offset:6144
	ds_read_b128 v[50:53], v209 offset:6144
	s_cmp_lt_i32 s83, 0
	s_cbranch_scc1 .Lbm_g2_end_a
	v_mbcnt_lo_u32_b32 v80, s22, 0
	v_mbcnt_hi_u32_b32 v80, s23, v80
	s_lshl_b32 s32, s91, 2
	v_mov_b32_e32 v199, -1
	s_add_i32 s77, s32, 0
	v_cmp_eq_u32_e64 s[84:85], s77, v80
	s_nop 3
	s_and_b64 s[84:85], s[84:85], s[22:23]
	s_ff1_i32_b64 s77, s[84:85]
	v_writelane_b32 v199, s77, 0
	s_add_i32 s77, s32, 1
	v_cmp_eq_u32_e64 s[84:85], s77, v80
	s_nop 3
	s_and_b64 s[84:85], s[84:85], s[22:23]
	s_ff1_i32_b64 s77, s[84:85]
	v_writelane_b32 v199, s77, 1
	s_add_i32 s77, s32, 2
	v_cmp_eq_u32_e64 s[84:85], s77, v80
	s_nop 3
	s_and_b64 s[84:85], s[84:85], s[22:23]
	s_ff1_i32_b64 s77, s[84:85]
	v_writelane_b32 v199, s77, 2
	s_add_i32 s77, s32, 3
	v_cmp_eq_u32_e64 s[84:85], s77, v80
	s_nop 3
	s_and_b64 s[84:85], s[84:85], s[22:23]
	s_ff1_i32_b64 s77, s[84:85]
	v_writelane_b32 v199, s77, 3
	ds_bpermute_b32 v251, v250, v199
	s_waitcnt lgkmcnt(0)
; __device__ __forceinline__ float ex2(float x) { return __builtin_amdgcn_exp2f(x); }
; template <bool SELMASK>
; __device__ __forceinline__ void attn_far_fast(const LAS unsigned char* kb, const LAS unsigned char* vb, const bf16x8 (&qf)[2][2], int col, int q, float bias_far, bool sel0, bool sel1, Softmax (&st)[2], f32x4 (&O)[2][4]) {
;     ...
;     bf16x8 pf[2][2];
; #pragma unroll
;     for (int c = 0; c < 2; ++c) {
;         const bool sel = c == 0 ? sel0 : sel1;
;         const float off = ((SELMASK && !sel) ? NEG : bias_far) - st[c].m;
; #pragma unroll
;         for (int kt = 0; kt < 4; ++kt) { f32x4 p = S[c][kt] + off;
; #pragma unroll
;             for (int e = 0; e < 4; ++e) p[e] = ex2(p[e]);
;             S[c][kt] = p; }
;         pf[c][0] = pack8(S[c][0], S[c][1]); pf[c][1] = pack8(S[c][2], S[c][3]);
;         st[c].l = __builtin_amdgcn_mfma_f32_16x16x32_bf16(ONES8, pf[c][0], st[c].l, 0, 0, 0); st[c].l = __builtin_amdgcn_mfma_f32_16x16x32_bf16(ONES8, pf[c][1], st[c].l, 0, 0, 0);
;     }
; #pragma unroll
;     for (int c32 = 0; c32 < 2; ++c32)
; #pragma unroll
;         for (int dt = 0; dt < 4; ++dt) { const bf16x8 vf = lds_frag(vb, 16 * dt + col, 4 * c32 + q);
;             O[0][dt] = __builtin_amdgcn_mfma_f32_16x16x32_bf16(vf, pf[0][c32], O[0][dt], 0, 0, 0);
;             O[1][dt] = __builtin_amdgcn_mfma_f32_16x16x32_bf16(vf, pf[1][c32], O[1][dt], 0, 0, 0); }
.Lbm_g2_end_a:
	v_exp_f32_e32 v70, v70
	v_exp_f32_e32 v71, v71
	v_exp_f32_e32 v72, v72
	v_exp_f32_e32 v73, v73
	v_exp_f32_e32 v74, v74
	v_exp_f32_e32 v75, v75
	v_exp_f32_e32 v76, v76
	v_exp_f32_e32 v77, v77
	v_exp_f32_e32 v200, v200
	v_exp_f32_e32 v201, v201
	v_exp_f32_e32 v202, v202
	v_exp_f32_e32 v203, v203
	v_exp_f32_e32 v204, v204
	v_exp_f32_e32 v205, v205
	v_exp_f32_e32 v206, v206
	v_exp_f32_e32 v207, v207
	s_nop 0
	v_cvt_pk_bf16_f32 v70, v70, v71
	v_cvt_pk_bf16_f32 v71, v72, v73
	v_cvt_pk_bf16_f32 v72, v74, v75
	v_cvt_pk_bf16_f32 v73, v76, v77
	v_cvt_pk_bf16_f32 v74, v200, v201
	v_cvt_pk_bf16_f32 v75, v202, v203
	v_cvt_pk_bf16_f32 v76, v204, v205
	v_cvt_pk_bf16_f32 v77, v206, v207
	s_nop 1
	v_mfma_f32_16x16x32_bf16 v[100:103], v[112:115], v[70:73], 0
	v_mfma_f32_16x16x32_bf16 v[100:103], v[112:115], v[74:77], v[100:103]
	s_waitcnt lgkmcnt(4)
	v_mfma_f32_16x16x32_bf16 v[84:87], v[116:119], v[70:73], 0
	v_mfma_f32_16x16x32_bf16 v[84:87], v[120:123], v[74:77], v[84:87]
	v_mfma_f32_16x16x32_bf16 v[88:91], v[124:127], v[70:73], 0
	v_mfma_f32_16x16x32_bf16 v[88:91], v[128:131], v[74:77], v[88:91]
	v_mfma_f32_16x16x32_bf16 v[92:95], v[132:135], v[70:73], 0
	v_mfma_f32_16x16x32_bf16 v[92:95], v[136:139], v[74:77], v[92:95]
	v_mfma_f32_16x16x32_bf16 v[96:99], v[140:143], v[70:73], 0
	v_mfma_f32_16x16x32_bf16 v[96:99], v[144:147], v[74:77], v[96:99]
	s_waitcnt lgkmcnt(2)
	v_mfma_f32_16x16x32_bf16 v[62:65], v[38:41], v[104:107], v[62:65]
	v_mfma_f32_16x16x32_bf16 v[62:65], v[42:45], v[108:111], v[62:65]
	s_waitcnt lgkmcnt(0)
	v_mfma_f32_16x16x32_bf16 v[66:69], v[46:49], v[104:107], v[66:69]
	v_mfma_f32_16x16x32_bf16 v[66:69], v[50:53], v[108:111], v[66:69]
	ds_read_b128 v[116:119], v208 offset:32768
	ds_read_b128 v[120:123], v209 offset:32768
	ds_read_b128 v[124:127], v208 offset:34816
	ds_read_b128 v[128:131], v209 offset:34816
	ds_read_b128 v[132:135], v208 offset:36864
	ds_read_b128 v[136:139], v209 offset:36864
	ds_read_b128 v[140:143], v208 offset:38912
	ds_read_b128 v[144:147], v209 offset:38912
	s_mov_b32 s100, -1
	s_cmp_lt_i32 s83, 0
	s_cbranch_scc1 .Lbm_pi_end_a
	v_max_i32_e32 v254, 0, v251
	v_lshlrev_b32_e32 v254, 11, v254
	v_mov_b32_e32 v255, 0
	v_lshl_add_u64 v[254:255], v[254:255], 0, v[246:247]
	global_load_dwordx4 v[104:107], v[254:255], off
	global_load_dwordx4 v[108:111], v[254:255], off offset:64
	s_mov_b32 s100, s83
.Lbm_pi_end_a:
	v_exp_f32_e32 v54, v54
	v_exp_f32_e32 v55, v55
	v_exp_f32_e32 v56, v56
	v_exp_f32_e32 v57, v57
	v_exp_f32_e32 v58, v58
	v_exp_f32_e32 v59, v59
	v_exp_f32_e32 v60, v60
	v_exp_f32_e32 v61, v61
	v_exp_f32_e32 v62, v62
	v_exp_f32_e32 v63, v63
	v_exp_f32_e32 v64, v64
	v_exp_f32_e32 v65, v65
	v_exp_f32_e32 v66, v66
	v_exp_f32_e32 v67, v67
	v_exp_f32_e32 v68, v68
	v_exp_f32_e32 v69, v69
	s_nop 0
	v_cvt_pk_bf16_f32 v54, v54, v55
	v_cvt_pk_bf16_f32 v55, v56, v57
	v_cvt_pk_bf16_f32 v56, v58, v59
	v_cvt_pk_bf16_f32 v57, v60, v61
	v_cvt_pk_bf16_f32 v58, v62, v63
	v_cvt_pk_bf16_f32 v59, v64, v65
	v_cvt_pk_bf16_f32 v60, v66, v67
	v_cvt_pk_bf16_f32 v61, v68, v69
	s_nop 1
	v_mfma_f32_16x16x32_bf16 v[100:103], v[112:115], v[54:57], v[100:103]
	v_mfma_f32_16x16x32_bf16 v[100:103], v[112:115], v[58:61], v[100:103]
	s_waitcnt lgkmcnt(4)
	v_mfma_f32_16x16x32_bf16 v[84:87], v[116:119], v[54:57], v[84:87]
	v_mfma_f32_16x16x32_bf16 v[84:87], v[120:123], v[58:61], v[84:87]
	v_mfma_f32_16x16x32_bf16 v[88:91], v[124:127], v[54:57], v[88:91]
	v_mfma_f32_16x16x32_bf16 v[88:91], v[128:131], v[58:61], v[88:91]
	v_lshlrev_b32_e32 v254, 6, v186
	v_sub_u32_e32 v254, v83, v254
	ds_read_b32 v200, v83
	ds_read_b32 v201, v83 offset:16
	ds_read_b32 v202, v83 offset:32
	ds_read_b32 v203, v83 offset:48
	ds_read_b32 v204, v83 offset:256
	ds_read_b32 v205, v83 offset:272
	ds_read_b32 v206, v83 offset:288
	ds_read_b32 v207, v83 offset:304
	ds_read_b32 v199, v254 offset:1024
	s_waitcnt lgkmcnt(9)
	v_mfma_f32_16x16x32_bf16 v[92:95], v[132:135], v[54:57], v[92:95]
	v_mfma_f32_16x16x32_bf16 v[92:95], v[136:139], v[58:61], v[92:95]
	v_mfma_f32_16x16x32_bf16 v[96:99], v[140:143], v[54:57], v[96:99]
	v_mfma_f32_16x16x32_bf16 v[96:99], v[144:147], v[58:61], v[96:99]
	s_waitcnt lgkmcnt(7)
	ds_read_b32 v62, v83 offset:512
	ds_read_b32 v63, v83 offset:528
	ds_read_b32 v64, v83 offset:544
	ds_read_b32 v65, v83 offset:560
	ds_read_b32 v66, v83 offset:768
	ds_read_b32 v67, v83 offset:784
	ds_read_b32 v68, v83 offset:800
	ds_read_b32 v69, v83 offset:816
	s_waitcnt lgkmcnt(8)
	v_add_f32_e32 v200, v200, v84
	v_add_f32_e32 v201, v201, v85
	v_add_f32_e32 v202, v202, v86
	v_add_f32_e32 v203, v203, v87
	v_add_f32_e32 v204, v204, v88
	v_add_f32_e32 v205, v205, v89
	v_add_f32_e32 v206, v206, v90
	v_add_f32_e32 v207, v207, v91
	v_add_f32_e32 v199, v199, v100
	s_waitcnt lgkmcnt(0)
	v_add_f32_e32 v62, v62, v92
	v_add_f32_e32 v63, v63, v93
	v_add_f32_e32 v64, v64, v94
	v_add_f32_e32 v65, v65, v95
	v_add_f32_e32 v66, v66, v96
	v_add_f32_e32 v67, v67, v97
	v_add_f32_e32 v68, v68, v98
	v_add_f32_e32 v69, v69, v99
	v_cmp_ne_u32_e32 vcc, 0, v79
	s_and_saveexec_b64 s[84:85], vcc
	ds_write_b32 v83, v200
	ds_write_b32 v83, v201 offset:16
	ds_write_b32 v83, v202 offset:32
	ds_write_b32 v83, v203 offset:48
	ds_write_b32 v83, v204 offset:256
	ds_write_b32 v83, v205 offset:272
	ds_write_b32 v83, v206 offset:288
	ds_write_b32 v83, v207 offset:304
	ds_write_b32 v254, v199 offset:1024
	s_waitcnt lgkmcnt(7)
	ds_write_b32 v83, v62 offset:512
	ds_write_b32 v83, v63 offset:528
	ds_write_b32 v83, v64 offset:544
	ds_write_b32 v83, v65 offset:560
	ds_write_b32 v83, v66 offset:768
	ds_write_b32 v83, v67 offset:784
	ds_write_b32 v83, v68 offset:800
	ds_write_b32 v83, v69 offset:816
	s_mov_b64 exec, s[84:85]
	s_nop 3
	s_branch .Lbm_done
; #define LAS __attribute__((address_space(3)))
; __device__ __forceinline__ float ex2(float x) { return __builtin_amdgcn_exp2f(x); }
; template <bool SELMASK>
; __device__ __forceinline__ void attn_far_fast(const LAS unsigned char* kb, const LAS unsigned char* vb, const bf16x8 (&qf)[2][2], int col, int q, float bias_far, bool sel0, bool sel1, Softmax (&st)[2], f32x4 (&O)[2][4]) {
;     const f32x4 z4 = (f32x4){0.f, 0.f, 0.f, 0.f};
;     const float NEG = -__builtin_inff();
;     f32x4 S[2][4];
; #pragma unroll
;     for (int kt = 0; kt < 4; ++kt) { const bf16x8 k0 = lds_frag(kb, 16 * kt + col, q), k1 = lds_frag(kb, 16 * kt + col, 4 + q);
; #pragma unroll
;         for (int c = 0; c < 2; ++c) { S[c][kt] = __builtin_amdgcn_mfma_f32_16x16x32_bf16(k0, qf[c][0], z4, 0, 0, 0); S[c][kt] = __builtin_amdgcn_mfma_f32_16x16x32_bf16(k1, qf[c][1], S[c][kt], 0, 0, 0); } }
;     bf16x8 pf[2][2];
; #pragma unroll
;     for (int c = 0; c < 2; ++c) {
;         const bool sel = c == 0 ? sel0 : sel1;
;         const float off = ((SELMASK && !sel) ? NEG : bias_far) - st[c].m;
; #pragma unroll
;         for (int kt = 0; kt < 4; ++kt) { f32x4 p = S[c][kt] + off;
; #pragma unroll
;             for (int e = 0; e < 4; ++e) p[e] = ex2(p[e]);
;             S[c][kt] = p; }
;         pf[c][0] = pack8(S[c][0], S[c][1]); pf[c][1] = pack8(S[c][2], S[c][3]);
;         st[c].l = __builtin_amdgcn_mfma_f32_16x16x32_bf16(ONES8, pf[c][0], st[c].l, 0, 0, 0); st[c].l = __builtin_amdgcn_mfma_f32_16x16x32_bf16(ONES8, pf[c][1], st[c].l, 0, 0, 0);
;     }
; #pragma unroll
;     for (int c32 = 0; c32 < 2; ++c32)
; #pragma unroll
;         for (int dt = 0; dt < 4; ++dt) { const bf16x8 vf = lds_frag(vb, 16 * dt + col, 4 * c32 + q);
;             O[0][dt] = __builtin_amdgcn_mfma_f32_16x16x32_bf16(vf, pf[0][c32], O[0][dt], 0, 0, 0);
;             O[1][dt] = __builtin_amdgcn_mfma_f32_16x16x32_bf16(vf, pf[1][c32], O[1][dt], 0, 0, 0); }
.Lbm_r1_two:
	v_add_u32_e32 v148, s83, v192
	v_add_u32_e32 v149, v148, v195
	v_add_u32_e32 v148, v148, v193
	v_add_u32_e32 v208, s99, v192
	v_add_u32_e32 v209, v208, v195
	v_add_u32_e32 v208, v208, v193
	ds_read_b128 v[116:119], v148
	ds_read_b128 v[120:123], v149
	ds_read_b128 v[124:127], v148 offset:2048
	ds_read_b128 v[128:131], v149 offset:2048
	ds_read_b128 v[132:135], v148 offset:4096
	ds_read_b128 v[136:139], v149 offset:4096
	ds_read_b128 v[140:143], v148 offset:6144
	ds_read_b128 v[144:147], v149 offset:6144
	v_mov_b32_e32 v70, v81
	v_mov_b32_e32 v71, v81
	v_mov_b32_e32 v72, v81
	v_mov_b32_e32 v73, v81
	v_mov_b32_e32 v74, v81
	v_mov_b32_e32 v75, v81
	v_mov_b32_e32 v76, v81
	v_mov_b32_e32 v77, v81
	v_mov_b32_e32 v200, v81
	v_mov_b32_e32 v201, v81
	v_mov_b32_e32 v202, v81
	v_mov_b32_e32 v203, v81
	v_mov_b32_e32 v204, v81
	v_mov_b32_e32 v205, v81
	v_mov_b32_e32 v206, v81
	v_mov_b32_e32 v207, v81
	ds_read_b128 v[38:41], v208
	ds_read_b128 v[42:45], v209
	ds_read_b128 v[46:49], v208 offset:2048
	ds_read_b128 v[50:53], v209 offset:2048
	v_mov_b32_e32 v54, v82
	v_mov_b32_e32 v55, v82
	v_mov_b32_e32 v56, v82
	v_mov_b32_e32 v57, v82
	v_mov_b32_e32 v58, v82
	v_mov_b32_e32 v59, v82
	v_mov_b32_e32 v60, v82
	v_mov_b32_e32 v61, v82
	v_mov_b32_e32 v62, v82
	v_mov_b32_e32 v63, v82
	v_mov_b32_e32 v64, v82
	v_mov_b32_e32 v65, v82
	v_mov_b32_e32 v66, v82
	v_mov_b32_e32 v67, v82
	v_mov_b32_e32 v68, v82
	v_mov_b32_e32 v69, v82
	s_waitcnt lgkmcnt(10)
	v_mfma_f32_16x16x32_bf16 v[70:73], v[116:119], v[104:107], v[70:73]
	v_mfma_f32_16x16x32_bf16 v[70:73], v[120:123], v[108:111], v[70:73]
	s_waitcnt lgkmcnt(8)
	v_mfma_f32_16x16x32_bf16 v[74:77], v[124:127], v[104:107], v[74:77]
	v_mfma_f32_16x16x32_bf16 v[74:77], v[128:131], v[108:111], v[74:77]
	ds_read_b128 v[116:119], v148 offset:32768
	ds_read_b128 v[120:123], v149 offset:32768
	ds_read_b128 v[124:127], v148 offset:34816
	ds_read_b128 v[128:131], v149 offset:34816
	s_waitcnt lgkmcnt(10)
	v_mfma_f32_16x16x32_bf16 v[200:203], v[132:135], v[104:107], v[200:203]
	v_mfma_f32_16x16x32_bf16 v[200:203], v[136:139], v[108:111], v[200:203]
	s_waitcnt lgkmcnt(8)
	v_mfma_f32_16x16x32_bf16 v[204:207], v[140:143], v[104:107], v[204:207]
	v_mfma_f32_16x16x32_bf16 v[204:207], v[144:147], v[108:111], v[204:207]
	ds_read_b128 v[132:135], v148 offset:36864
	ds_read_b128 v[136:139], v149 offset:36864
	ds_read_b128 v[140:143], v148 offset:38912
	ds_read_b128 v[144:147], v149 offset:38912
	s_waitcnt lgkmcnt(10)
	v_mfma_f32_16x16x32_bf16 v[54:57], v[38:41], v[104:107], v[54:57]
	v_mfma_f32_16x16x32_bf16 v[54:57], v[42:45], v[108:111], v[54:57]
	s_waitcnt lgkmcnt(8)
	v_mfma_f32_16x16x32_bf16 v[58:61], v[46:49], v[104:107], v[58:61]
	v_mfma_f32_16x16x32_bf16 v[58:61], v[50:53], v[108:111], v[58:61]
	ds_read_b128 v[38:41], v208 offset:4096
	ds_read_b128 v[42:45], v209 offset:4096
	ds_read_b128 v[46:49], v208 offset:6144
	ds_read_b128 v[50:53], v209 offset:6144
	v_exp_f32_e32 v70, v70
	v_exp_f32_e32 v71, v71
	v_exp_f32_e32 v72, v72
	v_exp_f32_e32 v73, v73
	v_exp_f32_e32 v74, v74
	v_exp_f32_e32 v75, v75
	v_exp_f32_e32 v76, v76
	v_exp_f32_e32 v77, v77
	v_exp_f32_e32 v200, v200
	v_exp_f32_e32 v201, v201
	v_exp_f32_e32 v202, v202
	v_exp_f32_e32 v203, v203
	v_exp_f32_e32 v204, v204
	v_exp_f32_e32 v205, v205
	v_exp_f32_e32 v206, v206
	v_exp_f32_e32 v207, v207
	s_nop 0
	v_cvt_pk_bf16_f32 v70, v70, v71
	v_cvt_pk_bf16_f32 v71, v72, v73
	v_cvt_pk_bf16_f32 v72, v74, v75
	v_cvt_pk_bf16_f32 v73, v76, v77
	v_cvt_pk_bf16_f32 v74, v200, v201
	v_cvt_pk_bf16_f32 v75, v202, v203
	v_cvt_pk_bf16_f32 v76, v204, v205
	v_cvt_pk_bf16_f32 v77, v206, v207
	s_nop 1
	v_mfma_f32_16x16x32_bf16 v[100:103], v[112:115], v[70:73], 0
	v_mfma_f32_16x16x32_bf16 v[100:103], v[112:115], v[74:77], v[100:103]
	s_waitcnt lgkmcnt(4)
	v_mfma_f32_16x16x32_bf16 v[84:87], v[116:119], v[70:73], 0
	v_mfma_f32_16x16x32_bf16 v[84:87], v[120:123], v[74:77], v[84:87]
	v_mfma_f32_16x16x32_bf16 v[88:91], v[124:127], v[70:73], 0
	v_mfma_f32_16x16x32_bf16 v[88:91], v[128:131], v[74:77], v[88:91]
	v_mfma_f32_16x16x32_bf16 v[92:95], v[132:135], v[70:73], 0
	v_mfma_f32_16x16x32_bf16 v[92:95], v[136:139], v[74:77], v[92:95]
	v_mfma_f32_16x16x32_bf16 v[96:99], v[140:143], v[70:73], 0
	v_mfma_f32_16x16x32_bf16 v[96:99], v[144:147], v[74:77], v[96:99]
	s_waitcnt lgkmcnt(2)
	v_mfma_f32_16x16x32_bf16 v[62:65], v[38:41], v[104:107], v[62:65]
	v_mfma_f32_16x16x32_bf16 v[62:65], v[42:45], v[108:111], v[62:65]
	s_waitcnt lgkmcnt(0)
	v_mfma_f32_16x16x32_bf16 v[66:69], v[46:49], v[104:107], v[66:69]
	v_mfma_f32_16x16x32_bf16 v[66:69], v[50:53], v[108:111], v[66:69]
	ds_read_b128 v[116:119], v208 offset:32768
	ds_read_b128 v[120:123], v209 offset:32768
	ds_read_b128 v[124:127], v208 offset:34816
	ds_read_b128 v[128:131], v209 offset:34816
	ds_read_b128 v[132:135], v208 offset:36864
	ds_read_b128 v[136:139], v209 offset:36864
	ds_read_b128 v[140:143], v208 offset:38912
	ds_read_b128 v[144:147], v209 offset:38912
	s_nop 3
	v_exp_f32_e32 v54, v54
	v_exp_f32_e32 v55, v55
	v_exp_f32_e32 v56, v56
	v_exp_f32_e32 v57, v57
	v_exp_f32_e32 v58, v58
	v_exp_f32_e32 v59, v59
	v_exp_f32_e32 v60, v60
	v_exp_f32_e32 v61, v61
	v_exp_f32_e32 v62, v62
	v_exp_f32_e32 v63, v63
	v_exp_f32_e32 v64, v64
	v_exp_f32_e32 v65, v65
	v_exp_f32_e32 v66, v66
	v_exp_f32_e32 v67, v67
	v_exp_f32_e32 v68, v68
	v_exp_f32_e32 v69, v69
	s_nop 0
	v_cvt_pk_bf16_f32 v54, v54, v55
	v_cvt_pk_bf16_f32 v55, v56, v57
	v_cvt_pk_bf16_f32 v56, v58, v59
	v_cvt_pk_bf16_f32 v57, v60, v61
	v_cvt_pk_bf16_f32 v58, v62, v63
	v_cvt_pk_bf16_f32 v59, v64, v65
	v_cvt_pk_bf16_f32 v60, v66, v67
	v_cvt_pk_bf16_f32 v61, v68, v69
	s_nop 1
	v_mfma_f32_16x16x32_bf16 v[100:103], v[112:115], v[54:57], v[100:103]
	v_mfma_f32_16x16x32_bf16 v[100:103], v[112:115], v[58:61], v[100:103]
	s_waitcnt lgkmcnt(4)
; #define LAS __attribute__((address_space(3)))
; __device__ __forceinline__ float ex2(float x) { return __builtin_amdgcn_exp2f(x); }
; template <bool SELMASK>
; __device__ __forceinline__ void attn_far_fast(const LAS unsigned char* kb, const LAS unsigned char* vb, const bf16x8 (&qf)[2][2], int col, int q, float bias_far, bool sel0, bool sel1, Softmax (&st)[2], f32x4 (&O)[2][4]) {
;     const f32x4 z4 = (f32x4){0.f, 0.f, 0.f, 0.f};
;     const float NEG = -__builtin_inff();
;     f32x4 S[2][4];
; #pragma unroll
;     for (int kt = 0; kt < 4; ++kt) { const bf16x8 k0 = lds_frag(kb, 16 * kt + col, q), k1 = lds_frag(kb, 16 * kt + col, 4 + q);
; #pragma unroll
;         for (int c = 0; c < 2; ++c) { S[c][kt] = __builtin_amdgcn_mfma_f32_16x16x32_bf16(k0, qf[c][0], z4, 0, 0, 0); S[c][kt] = __builtin_amdgcn_mfma_f32_16x16x32_bf16(k1, qf[c][1], S[c][kt], 0, 0, 0); } }
;     bf16x8 pf[2][2];
; #pragma unroll
;     for (int c = 0; c < 2; ++c) {
;         const bool sel = c == 0 ? sel0 : sel1;
;         const float off = ((SELMASK && !sel) ? NEG : bias_far) - st[c].m;
; #pragma unroll
;         for (int kt = 0; kt < 4; ++kt) { f32x4 p = S[c][kt] + off;
; #pragma unroll
;             for (int e = 0; e < 4; ++e) p[e] = ex2(p[e]);
;             S[c][kt] = p; }
;         pf[c][0] = pack8(S[c][0], S[c][1]); pf[c][1] = pack8(S[c][2], S[c][3]);
;         st[c].l = __builtin_amdgcn_mfma_f32_16x16x32_bf16(ONES8, pf[c][0], st[c].l, 0, 0, 0); st[c].l = __builtin_amdgcn_mfma_f32_16x16x32_bf16(ONES8, pf[c][1], st[c].l, 0, 0, 0);
;     }
; #pragma unroll
;     for (int c32 = 0; c32 < 2; ++c32)
; #pragma unroll
;         for (int dt = 0; dt < 4; ++dt) { const bf16x8 vf = lds_frag(vb, 16 * dt + col, 4 * c32 + q);
;             O[0][dt] = __builtin_amdgcn_mfma_f32_16x16x32_bf16(vf, pf[0][c32], O[0][dt], 0, 0, 0);
;             O[1][dt] = __builtin_amdgcn_mfma_f32_16x16x32_bf16(vf, pf[1][c32], O[1][dt], 0, 0, 0); }
	v_mfma_f32_16x16x32_bf16 v[84:87], v[116:119], v[54:57], v[84:87]
	v_mfma_f32_16x16x32_bf16 v[84:87], v[120:123], v[58:61], v[84:87]
	v_mfma_f32_16x16x32_bf16 v[88:91], v[124:127], v[54:57], v[88:91]
	v_mfma_f32_16x16x32_bf16 v[88:91], v[128:131], v[58:61], v[88:91]
	v_lshlrev_b32_e32 v254, 6, v186
	v_sub_u32_e32 v254, v83, v254
	ds_read_b32 v200, v83
	ds_read_b32 v201, v83 offset:16
	ds_read_b32 v202, v83 offset:32
	ds_read_b32 v203, v83 offset:48
	ds_read_b32 v204, v83 offset:256
	ds_read_b32 v205, v83 offset:272
	ds_read_b32 v206, v83 offset:288
	ds_read_b32 v207, v83 offset:304
	ds_read_b32 v199, v254 offset:1024
	s_waitcnt lgkmcnt(9)
	v_mfma_f32_16x16x32_bf16 v[92:95], v[132:135], v[54:57], v[92:95]
	v_mfma_f32_16x16x32_bf16 v[92:95], v[136:139], v[58:61], v[92:95]
	v_mfma_f32_16x16x32_bf16 v[96:99], v[140:143], v[54:57], v[96:99]
	v_mfma_f32_16x16x32_bf16 v[96:99], v[144:147], v[58:61], v[96:99]
	s_waitcnt lgkmcnt(7)
	ds_read_b32 v62, v83 offset:512
	ds_read_b32 v63, v83 offset:528
	ds_read_b32 v64, v83 offset:544
	ds_read_b32 v65, v83 offset:560
	ds_read_b32 v66, v83 offset:768
	ds_read_b32 v67, v83 offset:784
	ds_read_b32 v68, v83 offset:800
	ds_read_b32 v69, v83 offset:816
	s_waitcnt lgkmcnt(8)
	v_add_f32_e32 v200, v200, v84
	v_add_f32_e32 v201, v201, v85
	v_add_f32_e32 v202, v202, v86
	v_add_f32_e32 v203, v203, v87
	v_add_f32_e32 v204, v204, v88
	v_add_f32_e32 v205, v205, v89
	v_add_f32_e32 v206, v206, v90
	v_add_f32_e32 v207, v207, v91
	v_add_f32_e32 v199, v199, v100
	s_waitcnt lgkmcnt(0)
	v_add_f32_e32 v62, v62, v92
	v_add_f32_e32 v63, v63, v93
	v_add_f32_e32 v64, v64, v94
	v_add_f32_e32 v65, v65, v95
	v_add_f32_e32 v66, v66, v96
	v_add_f32_e32 v67, v67, v97
	v_add_f32_e32 v68, v68, v98
	v_add_f32_e32 v69, v69, v99
	v_cmp_ne_u32_e32 vcc, 0, v79
	s_and_saveexec_b64 s[84:85], vcc
	ds_write_b32 v83, v200
	ds_write_b32 v83, v201 offset:16
	ds_write_b32 v83, v202 offset:32
	ds_write_b32 v83, v203 offset:48
	ds_write_b32 v83, v204 offset:256
	ds_write_b32 v83, v205 offset:272
	ds_write_b32 v83, v206 offset:288
	ds_write_b32 v83, v207 offset:304
	ds_write_b32 v254, v199 offset:1024
	s_waitcnt lgkmcnt(7)
	ds_write_b32 v83, v62 offset:512
	ds_write_b32 v83, v63 offset:528
	ds_write_b32 v83, v64 offset:544
	ds_write_b32 v83, v65 offset:560
	ds_write_b32 v83, v66 offset:768
	ds_write_b32 v83, v67 offset:784
	ds_write_b32 v83, v68 offset:800
	ds_write_b32 v83, v69 offset:816
	s_mov_b64 exec, s[84:85]
	s_nop 3
	s_mov_b32 s100, -1
	s_add_i32 s21, s91, 8
	s_lshl_b32 s32, s21, 2
	v_mov_b32_e32 v133, -1
	s_add_i32 s77, s32, 0
	v_cmp_eq_u32_e64 s[84:85], s77, v80
	s_nop 3
	s_and_b64 s[84:85], s[84:85], s[22:23]
	s_ff1_i32_b64 s77, s[84:85]
	v_writelane_b32 v133, s77, 0
	s_add_i32 s77, s32, 1
	v_cmp_eq_u32_e64 s[84:85], s77, v80
	s_nop 3
	s_and_b64 s[84:85], s[84:85], s[22:23]
	s_ff1_i32_b64 s77, s[84:85]
	v_writelane_b32 v133, s77, 1
	s_add_i32 s77, s32, 2
	v_cmp_eq_u32_e64 s[84:85], s77, v80
	s_nop 3
	s_and_b64 s[84:85], s[84:85], s[22:23]
	s_ff1_i32_b64 s77, s[84:85]
	v_writelane_b32 v133, s77, 2
	s_add_i32 s77, s32, 3
	v_cmp_eq_u32_e64 s[84:85], s77, v80
	s_nop 3
	s_and_b64 s[84:85], s[84:85], s[22:23]
	s_ff1_i32_b64 s77, s[84:85]
	v_writelane_b32 v133, s77, 3
	ds_bpermute_b32 v132, v250, v133
	s_waitcnt lgkmcnt(0)
	v_lshrrev_b32_e32 v134, 31, v132
	v_xor_b32_e32 v134, 1, v134
	v_mov_b32_e32 v79, v134
	v_max_i32_e32 v132, 0, v132
	v_lshlrev_b32_e32 v136, 11, v132
	v_mov_b32_e32 v137, 0
	v_lshl_add_u64 v[138:139], v[136:137], 0, v[246:247]
	global_load_dwordx4 v[104:107], v[138:139], off
	global_load_dwordx4 v[108:111], v[138:139], off offset:64
	v_lshl_add_u32 v141, v132, 4, v249
	ds_read_b32 v140, v141
	v_mul_u32_u24_e32 v83, 0x410, v132
	v_add_u32_e32 v83, v83, v248
	v_lshrrev_b64 v[136:137], v132, s[12:13]
	v_and_b32_e32 v136, v136, v134
	v_cmp_ne_u32_e32 vcc, 0, v136
	s_nop 1
	v_cndmask_b32_e32 v81, v2, v154, vcc
	v_lshrrev_b64 v[136:137], v132, s[14:15]
	v_and_b32_e32 v136, v136, v134
	v_cmp_ne_u32_e32 vcc, 0, v136
	s_nop 1
	v_cndmask_b32_e32 v82, v2, v154, vcc
	s_waitcnt lgkmcnt(0)
	v_sub_f32_e32 v81, v81, v140
	v_sub_f32_e32 v82, v82, v140
	s_waitcnt vmcnt(0)
	s_and_b32 s83, s1, 0x4000
	v_add_u32_e32 v148, s83, v192
	v_add_u32_e32 v149, v148, v195
	v_add_u32_e32 v148, v148, v193
	v_add_u32_e32 v208, s99, v192
	v_add_u32_e32 v209, v208, v195
	v_add_u32_e32 v208, v208, v193
	ds_read_b128 v[116:119], v148
	ds_read_b128 v[120:123], v149
	ds_read_b128 v[124:127], v148 offset:2048
	ds_read_b128 v[128:131], v149 offset:2048
	ds_read_b128 v[132:135], v148 offset:4096
	ds_read_b128 v[136:139], v149 offset:4096
	ds_read_b128 v[140:143], v148 offset:6144
	ds_read_b128 v[144:147], v149 offset:6144
	v_mov_b32_e32 v70, v81
	v_mov_b32_e32 v71, v81
	v_mov_b32_e32 v72, v81
	v_mov_b32_e32 v73, v81
	v_mov_b32_e32 v74, v81
	v_mov_b32_e32 v75, v81
	v_mov_b32_e32 v76, v81
	v_mov_b32_e32 v77, v81
	v_mov_b32_e32 v200, v81
	v_mov_b32_e32 v201, v81
	v_mov_b32_e32 v202, v81
	v_mov_b32_e32 v203, v81
	v_mov_b32_e32 v204, v81
	v_mov_b32_e32 v205, v81
	v_mov_b32_e32 v206, v81
	v_mov_b32_e32 v207, v81
	ds_read_b128 v[38:41], v208
	ds_read_b128 v[42:45], v209
	ds_read_b128 v[46:49], v208 offset:2048
	ds_read_b128 v[50:53], v209 offset:2048
	v_mov_b32_e32 v54, v82
	v_mov_b32_e32 v55, v82
	v_mov_b32_e32 v56, v82
	v_mov_b32_e32 v57, v82
	v_mov_b32_e32 v58, v82
	v_mov_b32_e32 v59, v82
	v_mov_b32_e32 v60, v82
	v_mov_b32_e32 v61, v82
	v_mov_b32_e32 v62, v82
	v_mov_b32_e32 v63, v82
	v_mov_b32_e32 v64, v82
	v_mov_b32_e32 v65, v82
	v_mov_b32_e32 v66, v82
	v_mov_b32_e32 v67, v82
	v_mov_b32_e32 v68, v82
	v_mov_b32_e32 v69, v82
	s_waitcnt lgkmcnt(10)
; #define LAS __attribute__((address_space(3)))
; __device__ __forceinline__ float ex2(float x) { return __builtin_amdgcn_exp2f(x); }
; template <bool SELMASK>
; __device__ __forceinline__ void attn_far_fast(const LAS unsigned char* kb, const LAS unsigned char* vb, const bf16x8 (&qf)[2][2], int col, int q, float bias_far, bool sel0, bool sel1, Softmax (&st)[2], f32x4 (&O)[2][4]) {
;     const f32x4 z4 = (f32x4){0.f, 0.f, 0.f, 0.f};
;     const float NEG = -__builtin_inff();
;     f32x4 S[2][4];
; #pragma unroll
;     for (int kt = 0; kt < 4; ++kt) { const bf16x8 k0 = lds_frag(kb, 16 * kt + col, q), k1 = lds_frag(kb, 16 * kt + col, 4 + q);
; #pragma unroll
;         for (int c = 0; c < 2; ++c) { S[c][kt] = __builtin_amdgcn_mfma_f32_16x16x32_bf16(k0, qf[c][0], z4, 0, 0, 0); S[c][kt] = __builtin_amdgcn_mfma_f32_16x16x32_bf16(k1, qf[c][1], S[c][kt], 0, 0, 0); } }
;     bf16x8 pf[2][2];
; #pragma unroll
;     for (int c = 0; c < 2; ++c) {
;         const bool sel = c == 0 ? sel0 : sel1;
;         const float off = ((SELMASK && !sel) ? NEG : bias_far) - st[c].m;
; #pragma unroll
;         for (int kt = 0; kt < 4; ++kt) { f32x4 p = S[c][kt] + off;
; #pragma unroll
;             for (int e = 0; e < 4; ++e) p[e] = ex2(p[e]);
;             S[c][kt] = p; }
;         pf[c][0] = pack8(S[c][0], S[c][1]); pf[c][1] = pack8(S[c][2], S[c][3]);
;         st[c].l = __builtin_amdgcn_mfma_f32_16x16x32_bf16(ONES8, pf[c][0], st[c].l, 0, 0, 0); st[c].l = __builtin_amdgcn_mfma_f32_16x16x32_bf16(ONES8, pf[c][1], st[c].l, 0, 0, 0);
;     }
; #pragma unroll
;     for (int c32 = 0; c32 < 2; ++c32)
; #pragma unroll
;         for (int dt = 0; dt < 4; ++dt) { const bf16x8 vf = lds_frag(vb, 16 * dt + col, 4 * c32 + q);
;             O[0][dt] = __builtin_amdgcn_mfma_f32_16x16x32_bf16(vf, pf[0][c32], O[0][dt], 0, 0, 0);
;             O[1][dt] = __builtin_amdgcn_mfma_f32_16x16x32_bf16(vf, pf[1][c32], O[1][dt], 0, 0, 0); }
	v_mfma_f32_16x16x32_bf16 v[70:73], v[116:119], v[104:107], v[70:73]
	v_mfma_f32_16x16x32_bf16 v[70:73], v[120:123], v[108:111], v[70:73]
	s_waitcnt lgkmcnt(8)
	v_mfma_f32_16x16x32_bf16 v[74:77], v[124:127], v[104:107], v[74:77]
	v_mfma_f32_16x16x32_bf16 v[74:77], v[128:131], v[108:111], v[74:77]
	ds_read_b128 v[116:119], v148 offset:32768
	ds_read_b128 v[120:123], v149 offset:32768
	ds_read_b128 v[124:127], v148 offset:34816
	ds_read_b128 v[128:131], v149 offset:34816
	s_waitcnt lgkmcnt(10)
	v_mfma_f32_16x16x32_bf16 v[200:203], v[132:135], v[104:107], v[200:203]
	v_mfma_f32_16x16x32_bf16 v[200:203], v[136:139], v[108:111], v[200:203]
	s_waitcnt lgkmcnt(8)
	v_mfma_f32_16x16x32_bf16 v[204:207], v[140:143], v[104:107], v[204:207]
	v_mfma_f32_16x16x32_bf16 v[204:207], v[144:147], v[108:111], v[204:207]
	ds_read_b128 v[132:135], v148 offset:36864
	ds_read_b128 v[136:139], v149 offset:36864
	ds_read_b128 v[140:143], v148 offset:38912
	ds_read_b128 v[144:147], v149 offset:38912
	s_waitcnt lgkmcnt(10)
	v_mfma_f32_16x16x32_bf16 v[54:57], v[38:41], v[104:107], v[54:57]
	v_mfma_f32_16x16x32_bf16 v[54:57], v[42:45], v[108:111], v[54:57]
	s_waitcnt lgkmcnt(8)
	v_mfma_f32_16x16x32_bf16 v[58:61], v[46:49], v[104:107], v[58:61]
	v_mfma_f32_16x16x32_bf16 v[58:61], v[50:53], v[108:111], v[58:61]
	ds_read_b128 v[38:41], v208 offset:4096
	ds_read_b128 v[42:45], v209 offset:4096
	ds_read_b128 v[46:49], v208 offset:6144
	ds_read_b128 v[50:53], v209 offset:6144
	v_exp_f32_e32 v70, v70
	v_exp_f32_e32 v71, v71
	v_exp_f32_e32 v72, v72
	v_exp_f32_e32 v73, v73
	v_exp_f32_e32 v74, v74
	v_exp_f32_e32 v75, v75
	v_exp_f32_e32 v76, v76
	v_exp_f32_e32 v77, v77
	v_exp_f32_e32 v200, v200
	v_exp_f32_e32 v201, v201
	v_exp_f32_e32 v202, v202
	v_exp_f32_e32 v203, v203
	v_exp_f32_e32 v204, v204
	v_exp_f32_e32 v205, v205
	v_exp_f32_e32 v206, v206
	v_exp_f32_e32 v207, v207
	s_nop 0
	v_cvt_pk_bf16_f32 v70, v70, v71
	v_cvt_pk_bf16_f32 v71, v72, v73
	v_cvt_pk_bf16_f32 v72, v74, v75
	v_cvt_pk_bf16_f32 v73, v76, v77
	v_cvt_pk_bf16_f32 v74, v200, v201
	v_cvt_pk_bf16_f32 v75, v202, v203
	v_cvt_pk_bf16_f32 v76, v204, v205
	v_cvt_pk_bf16_f32 v77, v206, v207
	s_nop 1
	v_mfma_f32_16x16x32_bf16 v[100:103], v[112:115], v[70:73], 0
	v_mfma_f32_16x16x32_bf16 v[100:103], v[112:115], v[74:77], v[100:103]
	s_waitcnt lgkmcnt(4)
	v_mfma_f32_16x16x32_bf16 v[84:87], v[116:119], v[70:73], 0
	v_mfma_f32_16x16x32_bf16 v[84:87], v[120:123], v[74:77], v[84:87]
	v_mfma_f32_16x16x32_bf16 v[88:91], v[124:127], v[70:73], 0
	v_mfma_f32_16x16x32_bf16 v[88:91], v[128:131], v[74:77], v[88:91]
	v_mfma_f32_16x16x32_bf16 v[92:95], v[132:135], v[70:73], 0
	v_mfma_f32_16x16x32_bf16 v[92:95], v[136:139], v[74:77], v[92:95]
	v_mfma_f32_16x16x32_bf16 v[96:99], v[140:143], v[70:73], 0
	v_mfma_f32_16x16x32_bf16 v[96:99], v[144:147], v[74:77], v[96:99]
	s_waitcnt lgkmcnt(2)
	v_mfma_f32_16x16x32_bf16 v[62:65], v[38:41], v[104:107], v[62:65]
	v_mfma_f32_16x16x32_bf16 v[62:65], v[42:45], v[108:111], v[62:65]
	s_waitcnt lgkmcnt(0)
	v_mfma_f32_16x16x32_bf16 v[66:69], v[46:49], v[104:107], v[66:69]
	v_mfma_f32_16x16x32_bf16 v[66:69], v[50:53], v[108:111], v[66:69]
	ds_read_b128 v[116:119], v208 offset:32768
	ds_read_b128 v[120:123], v209 offset:32768
	ds_read_b128 v[124:127], v208 offset:34816
	ds_read_b128 v[128:131], v209 offset:34816
	ds_read_b128 v[132:135], v208 offset:36864
	ds_read_b128 v[136:139], v209 offset:36864
	ds_read_b128 v[140:143], v208 offset:38912
	ds_read_b128 v[144:147], v209 offset:38912
	s_nop 3
	v_exp_f32_e32 v54, v54
	v_exp_f32_e32 v55, v55
	v_exp_f32_e32 v56, v56
	v_exp_f32_e32 v57, v57
	v_exp_f32_e32 v58, v58
	v_exp_f32_e32 v59, v59
	v_exp_f32_e32 v60, v60
	v_exp_f32_e32 v61, v61
	v_exp_f32_e32 v62, v62
	v_exp_f32_e32 v63, v63
	v_exp_f32_e32 v64, v64
	v_exp_f32_e32 v65, v65
	v_exp_f32_e32 v66, v66
	v_exp_f32_e32 v67, v67
	v_exp_f32_e32 v68, v68
	v_exp_f32_e32 v69, v69
	s_nop 0
	v_cvt_pk_bf16_f32 v54, v54, v55
	v_cvt_pk_bf16_f32 v55, v56, v57
	v_cvt_pk_bf16_f32 v56, v58, v59
	v_cvt_pk_bf16_f32 v57, v60, v61
	v_cvt_pk_bf16_f32 v58, v62, v63
	v_cvt_pk_bf16_f32 v59, v64, v65
	v_cvt_pk_bf16_f32 v60, v66, v67
	v_cvt_pk_bf16_f32 v61, v68, v69
	s_nop 1
	v_mfma_f32_16x16x32_bf16 v[100:103], v[112:115], v[54:57], v[100:103]
	v_mfma_f32_16x16x32_bf16 v[100:103], v[112:115], v[58:61], v[100:103]
	s_waitcnt lgkmcnt(4)
	v_mfma_f32_16x16x32_bf16 v[84:87], v[116:119], v[54:57], v[84:87]
	v_mfma_f32_16x16x32_bf16 v[84:87], v[120:123], v[58:61], v[84:87]
	v_mfma_f32_16x16x32_bf16 v[88:91], v[124:127], v[54:57], v[88:91]
	v_mfma_f32_16x16x32_bf16 v[88:91], v[128:131], v[58:61], v[88:91]
	v_lshlrev_b32_e32 v254, 6, v186
	v_sub_u32_e32 v254, v83, v254
	ds_read_b32 v200, v83
	ds_read_b32 v201, v83 offset:16
	ds_read_b32 v202, v83 offset:32
	ds_read_b32 v203, v83 offset:48
	ds_read_b32 v204, v83 offset:256
	ds_read_b32 v205, v83 offset:272
	ds_read_b32 v206, v83 offset:288
	ds_read_b32 v207, v83 offset:304
	ds_read_b32 v199, v254 offset:1024
	s_waitcnt lgkmcnt(9)
	v_mfma_f32_16x16x32_bf16 v[92:95], v[132:135], v[54:57], v[92:95]
	v_mfma_f32_16x16x32_bf16 v[92:95], v[136:139], v[58:61], v[92:95]
	v_mfma_f32_16x16x32_bf16 v[96:99], v[140:143], v[54:57], v[96:99]
	v_mfma_f32_16x16x32_bf16 v[96:99], v[144:147], v[58:61], v[96:99]
	s_waitcnt lgkmcnt(7)
	ds_read_b32 v62, v83 offset:512
	ds_read_b32 v63, v83 offset:528
	ds_read_b32 v64, v83 offset:544
	ds_read_b32 v65, v83 offset:560
	ds_read_b32 v66, v83 offset:768
	ds_read_b32 v67, v83 offset:784
	ds_read_b32 v68, v83 offset:800
	ds_read_b32 v69, v83 offset:816
	s_waitcnt lgkmcnt(8)
	v_add_f32_e32 v200, v200, v84
	v_add_f32_e32 v201, v201, v85
	v_add_f32_e32 v202, v202, v86
	v_add_f32_e32 v203, v203, v87
	v_add_f32_e32 v204, v204, v88
	v_add_f32_e32 v205, v205, v89
	v_add_f32_e32 v206, v206, v90
	v_add_f32_e32 v207, v207, v91
	v_add_f32_e32 v199, v199, v100
	s_waitcnt lgkmcnt(0)
	v_add_f32_e32 v62, v62, v92
	v_add_f32_e32 v63, v63, v93
	v_add_f32_e32 v64, v64, v94
	v_add_f32_e32 v65, v65, v95
	v_add_f32_e32 v66, v66, v96
	v_add_f32_e32 v67, v67, v97
	v_add_f32_e32 v68, v68, v98
	v_add_f32_e32 v69, v69, v99
	v_cmp_ne_u32_e32 vcc, 0, v79
	s_and_saveexec_b64 s[84:85], vcc
	ds_write_b32 v83, v200
	ds_write_b32 v83, v201 offset:16
	ds_write_b32 v83, v202 offset:32
	ds_write_b32 v83, v203 offset:48
	ds_write_b32 v83, v204 offset:256
	ds_write_b32 v83, v205 offset:272
	ds_write_b32 v83, v206 offset:288
	ds_write_b32 v83, v207 offset:304
	ds_write_b32 v254, v199 offset:1024
	s_waitcnt lgkmcnt(7)
	ds_write_b32 v83, v62 offset:512
	ds_write_b32 v83, v63 offset:528
	ds_write_b32 v83, v64 offset:544
	ds_write_b32 v83, v65 offset:560
	ds_write_b32 v83, v66 offset:768
	ds_write_b32 v83, v67 offset:784
	ds_write_b32 v83, v68 offset:800
	ds_write_b32 v83, v69 offset:816
	s_mov_b64 exec, s[84:85]
	s_nop 3

.Lbm_pf_end_b:
.Lbm_join:
	s_add_i32 s10, s1, 0x4000
	s_and_b32 s10, s10, 0x4000
	v_add_u32_e32 v78, s10, v188
	s_cmp_lt_i32 s100, 0
	s_cbranch_scc1 .Lbm_join0
	s_waitcnt vmcnt(2)
	s_branch .Lbm_join1

.Lbm_join1:
	ds_write_b128 v78, v[26:29]
	ds_write_b128 v78, v[22:25] offset:32768
	s_add_i32 s10, s1, 0x6000
	s_and_b32 s10, s10, 0x6000
	v_add_u32_e32 v78, s10, v188
	ds_write_b128 v78, v[30:33]
	ds_write_b128 v78, v[34:37] offset:32768
	s_branch .LBB0_1228
